# P9 schedule-table counters read with a plain load after the grid barrier's agent-scope acquire (was an sc1 load by all 256 workgroups on the same two lines)
# speedup vs baseline: 1.0221x; 1.0026x over previous
.LBB0_852:
	s_load_dwordx8 s[40:47], s[0:1], 0xd8
	s_cmp_lt_i32 s56, 10
	s_cselect_b64 s[0:1], -1, 0
	s_cmp_gt_i32 s57, 9
	s_cselect_b64 s[2:3], -1, 0
	s_and_b64 s[0:1], s[0:1], s[2:3]
	v_writelane_b32 v246, s76, 2
	s_waitcnt lgkmcnt(0)
	s_add_u32 s76, s46, 0x8000
	s_addc_u32 s77, s47, 0
	s_add_u32 s2, s46, 0x33500000
	s_addc_u32 s3, s47, 0
	s_add_u32 s58, s52, 0x200
	s_addc_u32 s59, s53, 0
	s_add_u32 s68, s52, 0x1000
	s_addc_u32 s69, s53, 0
	s_add_u32 s70, s52, 0x1100
	s_addc_u32 s71, s53, 0
	s_add_u32 s72, s52, 0x1200
	s_addc_u32 s73, s53, 0
	s_add_u32 s74, s52, 0x1300
	s_addc_u32 s75, s53, 0
	s_cmp_eq_u32 s54, 15
	s_cselect_b64 s[4:5], -1, 0
	v_writelane_b32 v246, s4, 3
	s_cmp_eq_u32 s54, 14
	s_nop 0
	v_writelane_b32 v246, s5, 4
	s_cselect_b64 s[4:5], -1, 0
	v_writelane_b32 v246, s4, 5
	s_cmp_eq_u32 s54, 13
	s_nop 0
	v_writelane_b32 v246, s5, 6
	s_cselect_b64 s[4:5], -1, 0
	v_writelane_b32 v246, s4, 7
	s_cmp_eq_u32 s54, 12
	s_nop 0
	v_writelane_b32 v246, s5, 8
	s_cselect_b64 s[4:5], -1, 0
	v_writelane_b32 v246, s4, 9
	s_cmp_eq_u32 s54, 11
	s_nop 0
	v_writelane_b32 v246, s5, 10
	s_cselect_b64 s[4:5], -1, 0
	v_writelane_b32 v246, s4, 11
	s_cmp_eq_u32 s54, 10
	s_nop 0
	v_writelane_b32 v246, s5, 12
	s_cselect_b64 s[4:5], -1, 0
	v_writelane_b32 v246, s4, 13
	s_cmp_eq_u32 s54, 9
	s_nop 0
	v_writelane_b32 v246, s5, 14
	s_cselect_b64 s[4:5], -1, 0
	v_writelane_b32 v246, s4, 15
	s_cmp_eq_u32 s54, 8
	s_nop 0
	v_writelane_b32 v246, s5, 16
	s_cselect_b64 s[4:5], -1, 0
	v_writelane_b32 v246, s4, 17
	s_cmp_eq_u32 s54, 7
	s_nop 0
	v_writelane_b32 v246, s5, 18
	s_cselect_b64 s[4:5], -1, 0
	v_writelane_b32 v246, s4, 19
	s_cmp_eq_u32 s54, 6
	s_nop 0
	v_writelane_b32 v246, s5, 20
	s_cselect_b64 s[4:5], -1, 0
	v_writelane_b32 v246, s4, 21
	s_cmp_eq_u32 s54, 5
	s_nop 0
	v_writelane_b32 v246, s5, 22
	s_cselect_b64 s[4:5], -1, 0
	v_writelane_b32 v246, s4, 23
	s_cmp_eq_u32 s54, 4
	s_nop 0
	v_writelane_b32 v246, s5, 24
	s_cselect_b64 s[4:5], -1, 0
	v_writelane_b32 v246, s4, 25
	s_cmp_eq_u32 s54, 3
	s_nop 0
	v_writelane_b32 v246, s5, 26
	s_cselect_b64 s[4:5], -1, 0
	v_writelane_b32 v246, s4, 27
	s_cmp_eq_u32 s54, 2
	s_nop 0
	v_writelane_b32 v246, s5, 28
	s_cselect_b64 s[4:5], -1, 0
	v_writelane_b32 v246, s4, 29
	s_cmp_eq_u32 s54, 1
	s_nop 0
	v_writelane_b32 v246, s5, 30
	s_cselect_b64 s[4:5], -1, 0
	v_writelane_b32 v246, s4, 31
	s_cmp_eq_u32 s54, 0
	s_nop 0
	v_writelane_b32 v246, s5, 32
	s_cselect_b64 s[4:5], -1, 0
	v_writelane_b32 v246, s4, 33
	s_nop 1
	v_writelane_b32 v246, s5, 34
	s_lshl_b32 s4, s54, 8
	s_add_u32 s4, s52, s4
	s_addc_u32 s5, s53, 0
	s_add_u32 s6, s4, 0x1400
	s_addc_u32 s7, s5, 0
	s_add_u32 s60, s4, 0x2400
	s_addc_u32 s61, s5, 0
	s_add_u32 s4, s52, 0x3400
	v_writelane_b32 v246, s6, 35
	s_addc_u32 s5, s53, 0
	s_add_u32 s62, s52, 0x3500
	v_writelane_b32 v246, s7, 36
	v_writelane_b32 v246, s4, 37
	s_addc_u32 s63, s53, 0
	s_andn2_b64 vcc, exec, s[0:1]
	v_writelane_b32 v246, s5, 38
	s_cbranch_vccnz .LBB0_958
	s_waitcnt vmcnt(0)
	v_mov_b32_e32 v2, v0
	s_nop 0
	v_cmp_gt_i32_e32 vcc, 64, v2
	v_lshl_add_u32 v1, v2, 2, 0
	s_barrier
	s_and_saveexec_b64 s[0:1], vcc
	s_cbranch_execz .LBB0_855
	v_ashrrev_i32_e32 v3, 31, v2
	v_lshl_add_u64 v[4:5], v[2:3], 2, s[76:77]
	global_load_dword v3, v[4:5], off
	v_add_u32_e32 v4, 0x20440, v1
	s_waitcnt vmcnt(0)
	ds_write_b32 v4, v3
